# MLA: first four K fragments of the next step prefetched from LDS in the P.V phase (barrier waits vmcnt(2)), tile DMA requests moved to QK^T gaps 1-3
# speedup vs baseline: 1.0164x; 1.0042x over previous
; #define LAS __attribute__((address_space(3)))
; __device__ __forceinline__ float ex2(float x) { return __builtin_amdgcn_exp2f(x); }
; __device__ __forceinline__ f32x16 mfma32(bf16x8 a, bf16x8 b, f32x16 c) { return __builtin_amdgcn_mfma_f32_32x32x16_bf16(a, b, c, 0, 0, 0); }
; #define MLA_WAITBAR() do { if (wid < 4) asm volatile("s_waitcnt vmcnt(6) lgkmcnt(0)\n\ts_barrier" ::: "memory"); else asm volatile("s_waitcnt vmcnt(4) lgkmcnt(0)\n\ts_barrier" ::: "memory"); } while (0)
; #define MLA_ISSUE(s) do { const int tk_ = (s) + 3 < NT - 1 ? (s) + 3 : NT - 1, tv_ = (s) + 2 < 0 ? 0 : ((s) + 2 < NT - 1 ? (s) + 2 : NT - 1); MLA_DMAK(tk_, ((s) + 3) & 3); MLA_DMAV(tv_, ((s) + 2) & 3); } while (0)
; #define PIN(x) asm volatile("" : "+v"(x))
; __device__ __forceinline__ void mla_unit(int b, int h, int qb, const bf16_t* __restrict__ Q, const bf16_t* __restrict__ KV, const bf16_t* __restrict__ PROJ, bf16_t* OCAT, float* SSQO, ldsp shm) {
;     ...
;     MLA_WAITBAR();
;     MLA_ISSUE(0);
;     { const LAS unsigned char* kb = kp0; pA0 = f32x16{}; pA1 = f32x16{};
; #pragma unroll
;       for (int d0 = 0; d0 < 6; ++d0) { const bf16x8 k0 = *(const LAS bf16x8*)(kb + d0 * 2048), k1 = *(const LAS bf16x8*)(kb + d0 * 2048 + 512); pA0 = mfma32(k0, qr[d0], pA0); pA1 = mfma32(k1, qr[d0], pA1); }
;       mhat = rowmax(pA0, pA1);
; #pragma unroll
;       for (int r = 0; r < 16; ++r) { negm[r] = -mhat; pA0[r] = ex2(pA0[r] - mhat); pA1[r] = ex2(pA1[r] - mhat); } }
;     PIN(negm);
.LBB0_1145:
	s_mov_b64 s[10:11], 0x40000
	v_lshlrev_b32_e32 v6, 10, v184
	v_lshlrev_b32_e32 v7, 4, v183
	v_lshl_add_u64 v[4:5], v[4:5], 0, s[10:11]
	s_add_i32 m0, s26, 0x10000
	v_add3_u32 v188, 0, v6, v7
	global_load_lds_dwordx4 v[4:5], off
	ds_read_b128 v[4:7], v188
	ds_read_b128 v[10:13], v188 offset:512
	s_waitcnt vmcnt(0) lgkmcnt(0)
	v_mfma_f32_32x32x16_bf16 v[20:35], v[4:7], v[136:139], 0
	v_lshlrev_b32_e32 v9, 8, v184
	s_and_b32 s8, s2, 0x3fffffc0
	s_lshl_b32 s8, s8, 2
	s_add_i32 s51, s8, 0
	s_mov_b32 s8, s9
	s_mov_b32 s10, s9
	s_mov_b32 s11, s9
	v_mfma_f32_32x32x16_bf16 v[52:67], v[10:13], v[136:139], 0
	ds_read_b128 v[4:7], v188 offset:2048
	ds_read_b128 v[10:13], v188 offset:2560
	s_mov_b32 s12, s9
	s_mov_b32 s13, s9
	s_mov_b32 s14, s9
	s_mov_b32 s15, s9
	s_mov_b32 s16, s9
	s_mov_b32 s17, s9
	s_waitcnt lgkmcnt(1)
	v_mfma_f32_32x32x16_bf16 v[20:35], v[4:7], v[132:135], v[20:35]
	s_mov_b32 s18, s9
	s_mov_b32 s19, s9
	s_mov_b32 s20, s9
	s_mov_b32 s21, s9
	s_mov_b32 s22, s9
	s_mov_b32 s23, s9
	s_lshl_b32 s3, s3, 2
	s_waitcnt lgkmcnt(0)
	v_mfma_f32_32x32x16_bf16 v[52:67], v[10:13], v[132:135], v[52:67]
	ds_read_b128 v[4:7], v188 offset:4096
	ds_read_b128 v[10:13], v188 offset:4608
	s_ashr_i32 s2, s2, 7
	s_add_i32 s51, s51, 0x14000
	s_add_i32 s52, s2, s3
	s_mov_b32 s27, 2
	s_add_i32 s52, s52, 1
	s_or_b32 s2, s3, 3
	s_waitcnt lgkmcnt(1)
	v_mfma_f32_32x32x16_bf16 v[20:35], v[4:7], v[128:131], v[20:35]
	ds_read_b128 v[4:7], v188 offset:6144
	ds_read_b128 v[36:39], v188 offset:10752
	v_cmp_gt_u32_e64 s[36:37], 32, v182
	v_lshl_add_u32 v185, v183, 2, s51
	v_mov_b32_e32 v189, 0
	s_waitcnt lgkmcnt(2)
	v_mfma_f32_32x32x16_bf16 v[52:67], v[10:13], v[128:131], v[52:67]
	ds_read_b128 v[10:13], v188 offset:6656
	s_waitcnt lgkmcnt(2)
	v_mfma_f32_32x32x16_bf16 v[20:35], v[4:7], v[124:127], v[20:35]
	v_lshlrev_b32_e32 v4, 1, v1
	v_and_b32_e32 v4, 32, v4
	v_add3_u32 v8, 0, v4, v8
	v_lshlrev_b32_e32 v4, 4, v1
	v_and_b32_e32 v14, 0xc0, v4
	ds_read_b128 v[4:7], v188 offset:8192
	v_add3_u32 v186, v8, v9, v14
	s_waitcnt lgkmcnt(1)
	v_mfma_f32_32x32x16_bf16 v[52:67], v[10:13], v[124:127], v[52:67]
	ds_read_b128 v[8:11], v188 offset:8704
	s_waitcnt lgkmcnt(1)
	v_mfma_f32_32x32x16_bf16 v[20:35], v[4:7], v[120:123], v[20:35]
	ds_read_b128 v[4:7], v188 offset:10240
	s_waitcnt lgkmcnt(1)
	v_mfma_f32_32x32x16_bf16 v[52:67], v[8:11], v[120:123], v[52:67]
	s_waitcnt lgkmcnt(0)
	v_mfma_f32_32x32x16_bf16 v[20:35], v[4:7], v[116:119], v[20:35]
	v_mov_b64_e32 v[4:5], s[8:9]
	v_mov_b64_e32 v[18:19], s[22:23]
	v_mov_b64_e32 v[6:7], s[10:11]
	v_mov_b64_e32 v[8:9], s[12:13]
	v_mov_b64_e32 v[10:11], s[14:15]
	v_mov_b64_e32 v[12:13], s[16:17]
	v_mov_b64_e32 v[14:15], s[18:19]
	v_mfma_f32_32x32x16_bf16 v[52:67], v[36:39], v[116:119], v[52:67]
	s_nop 3
	v_max_f32_e32 v40, v21, v21
	v_max_f32_e32 v41, v20, v20
	v_max_f32_e32 v40, v41, v40
	v_mov_b64_e32 v[16:17], s[20:21]
	s_mov_b32 s14, 0x8000
	s_nop 2
	v_max3_f32 v36, v22, v23, v53
	v_max3_f32 v37, v40, v52, v54
	v_max3_f32 v37, v37, v55, v24
	v_max3_f32 v36, v36, v26, v27
	v_max3_f32 v37, v37, v25, v56
	v_max3_f32 v36, v36, v58, v59
	v_max3_f32 v37, v37, v57, v28
	v_max3_f32 v36, v36, v30, v31
	v_max3_f32 v37, v37, v29, v60
	v_max3_f32 v36, v36, v62, v63
	v_max3_f32 v37, v37, v61, v32
	v_max3_f32 v36, v36, v34, v35
	v_max3_f32 v37, v37, v33, v64
	v_max3_f32 v36, v36, v66, v67
	v_max3_f32 v36, v37, v65, v36
	v_mov_b32_e32 v37, v36
	s_nop 1
	v_permlane32_swap_b32_e32 v36, v37
	v_max_f32_e32 v37, v37, v37
	v_max_f32_e32 v36, v36, v36
	v_max_f32_e32 v187, v36, v37
	v_sub_f32_e32 v20, v20, v187
	v_exp_f32_e32 v68, v20
	v_sub_f32_e32 v20, v21, v187
	v_exp_f32_e32 v69, v20
	v_sub_f32_e32 v20, v22, v187
	v_exp_f32_e32 v70, v20
	v_sub_f32_e32 v20, v23, v187
	v_exp_f32_e32 v71, v20
	v_sub_f32_e32 v20, v24, v187
	v_exp_f32_e32 v72, v20
	v_sub_f32_e32 v20, v25, v187
	v_exp_f32_e32 v73, v20
	v_sub_f32_e32 v20, v26, v187
	v_exp_f32_e32 v74, v20
	v_sub_f32_e32 v20, v27, v187
	v_exp_f32_e32 v75, v20
	v_sub_f32_e32 v20, v28, v187
	v_exp_f32_e32 v76, v20
	v_sub_f32_e32 v20, v29, v187
	v_exp_f32_e32 v77, v20
	v_sub_f32_e32 v20, v30, v187
	v_exp_f32_e32 v78, v20
	v_sub_f32_e32 v20, v31, v187
	v_exp_f32_e32 v79, v20
	v_sub_f32_e32 v20, v32, v187
	v_exp_f32_e32 v80, v20
	v_sub_f32_e32 v20, v33, v187
	v_exp_f32_e32 v81, v20
	v_sub_f32_e32 v20, v34, v187
	v_sub_f32_e32 v52, v52, v187
	v_sub_f32_e32 v53, v53, v187
	v_sub_f32_e32 v54, v54, v187
	v_sub_f32_e32 v55, v55, v187
	v_sub_f32_e32 v56, v56, v187
	v_sub_f32_e32 v57, v57, v187
	v_sub_f32_e32 v58, v58, v187
	v_sub_f32_e32 v59, v59, v187
	v_sub_f32_e32 v60, v60, v187
	v_sub_f32_e32 v61, v61, v187
	v_sub_f32_e32 v62, v62, v187
	v_sub_f32_e32 v63, v63, v187
	v_sub_f32_e32 v64, v64, v187
	v_sub_f32_e32 v65, v65, v187
	v_sub_f32_e32 v66, v66, v187
	v_sub_f32_e32 v67, v67, v187
	v_exp_f32_e32 v82, v20
	v_sub_f32_e32 v20, v35, v187
	v_exp_f32_e32 v52, v52
	v_exp_f32_e32 v53, v53
	v_exp_f32_e32 v54, v54
	v_exp_f32_e32 v55, v55
	v_exp_f32_e32 v56, v56
	v_exp_f32_e32 v57, v57
	v_exp_f32_e32 v58, v58
	v_exp_f32_e32 v59, v59
	v_exp_f32_e32 v83, v20
	v_xor_b32_e32 v36, 0x80000000, v187
	v_mov_b64_e32 v[34:35], v[18:19]
	v_mov_b32_e32 v37, v36
	v_mov_b32_e32 v38, v36
	v_mov_b32_e32 v39, v36
	v_mov_b32_e32 v40, v36
	v_mov_b32_e32 v41, v36
	v_mov_b32_e32 v42, v36
	v_mov_b32_e32 v43, v36
	v_mov_b32_e32 v44, v36
	v_mov_b32_e32 v45, v36
	v_mov_b32_e32 v46, v36
	v_mov_b32_e32 v47, v36
	v_mov_b32_e32 v48, v36
	v_mov_b32_e32 v49, v36
	v_mov_b32_e32 v50, v36
	v_mov_b32_e32 v51, v36
	v_mov_b64_e32 v[32:33], v[16:17]
	v_mov_b64_e32 v[30:31], v[14:15]
	v_mov_b64_e32 v[28:29], v[12:13]
	v_mov_b64_e32 v[26:27], v[10:11]
	v_mov_b64_e32 v[24:25], v[8:9]
	v_mov_b64_e32 v[22:23], v[6:7]
	v_mov_b64_e32 v[20:21], v[4:5]
	s_add_i32 s12, s27, -1
	s_and_b32 s12, s12, 3
	s_mulk_i32 s12, 0x3000
	v_add_u32_e32 v156, s12, v188
	s_and_b32 s12, s14, 0x6000
	v_add_u32_e32 v157, s12, v186
	ds_read_b128 v[202:205], v156
	ds_read_b128 v[190:193], v156 offset:512
	ds_read_b128 v[194:197], v156 offset:2048
	ds_read_b128 v[198:201], v156 offset:2560
.LBB0_1146:
.LBB0_1147:
	s_waitcnt vmcnt(2) lgkmcnt(0)
	s_barrier
.LBB0_1149:
	s_setprio 1
	s_waitcnt lgkmcnt(0)
	v_mfma_f32_32x32x16_bf16 v[100:115], v[202:205], v[136:139], v[36:51]
	s_add_i32 s19, s27, -1
	s_and_b32 s18, s19, 3
	s_mul_i32 s20, s18, 0x3000
	s_and_b32 s17, s14, 0x6000
	s_add_i32 s16, s27, 2
	s_min_i32 s8, s16, s2
	s_lshl_b64 s[10:11], s[8:9], 17
	v_lshl_add_u64 v[154:155], v[176:177], 0, s[10:11]
	s_and_b32 s10, s16, 3
	s_mulk_i32 s10, 0x3000
	s_add_i32 s10, s26, s10
	s_mov_b32 m0, s10
	s_nop 0
	global_load_lds_dwordx4 v[154:155], off
	v_add_f32_e32 v88, v68, v69
	ds_read_b128 v[202:205], v156 offset:4096
	ds_read_b64_tr_b16 v[172:173], v157 offset:49152
	ds_read_b64_tr_b16 v[174:175], v157 offset:49664
	v_add_f32_e32 v84, v70, v88
	v_add_f32_e32 v84, v71, v84
	v_add_f32_e32 v84, v72, v84
	v_add_f32_e32 v144, v73, v84
	v_cvt_pk_bf16_f32 v140, v68, v69
	v_cvt_pk_bf16_f32 v141, v70, v71
	v_mfma_f32_32x32x16_bf16 v[84:99], v[190:193], v[136:139], v[36:51]
	s_and_b64 vcc, exec, s[38:39]
	s_cbranch_vccnz .Lmla_rope1
	s_lshl_b64 s[12:13], s[8:9], 18
	v_lshl_add_u64 v[154:155], v[180:181], 0, s[12:13]
	s_add_i32 m0, s10, 0x2000
	s_nop 0
	global_load_lds_dwordx4 v[154:155], off
.Lmla_rope1:
	ds_read_b128 v[190:193], v156 offset:4608
	ds_read_b64_tr_b16 v[68:69], v157 offset:53248
	ds_read_b64_tr_b16 v[70:71], v157 offset:53760
	v_add_f32_e32 v142, v74, v144
	v_add_f32_e32 v142, v75, v142
	v_add_f32_e32 v142, v76, v142
	v_add_f32_e32 v144, v77, v142
	v_cvt_pk_bf16_f32 v142, v72, v73
	v_cvt_pk_bf16_f32 v143, v74, v75
	v_mfma_f32_32x32x16_bf16 v[100:115], v[194:197], v[132:135], v[100:115]
	s_add_i32 s8, s27, 1
	s_min_i32 s8, s8, s2
	s_lshl_b32 s8, s8, 17
	v_lshl_add_u64 v[154:155], v[178:179], 0, s[8:9]
	s_add_i32 s8, s14, 0xffffe000
	s_and_b32 s15, s8, 0x6000
	s_add_i32 s8, s26, s15
	v_lshl_add_u64 v[154:155], v[154:155], 0, s[24:25]
	s_add_i32 m0, s8, 0xc000
	s_nop 0
	global_load_lds_dwordx4 v[154:155], off
	ds_read_b128 v[194:197], v156 offset:6144
	ds_read_b64_tr_b16 v[72:73], v157 offset:50176
	ds_read_b64_tr_b16 v[74:75], v157 offset:50688
	v_add_f32_e32 v144, v78, v144
	v_add_f32_e32 v144, v79, v144
	v_add_f32_e32 v144, v80, v144
	v_add_f32_e32 v148, v81, v144
	v_cvt_pk_bf16_f32 v144, v76, v77
	v_cvt_pk_bf16_f32 v145, v78, v79
	v_mfma_f32_32x32x16_bf16 v[84:99], v[198:201], v[132:135], v[84:99]
	ds_read_b128 v[198:201], v156 offset:6656
	ds_read_b64_tr_b16 v[76:77], v157 offset:54272
	ds_read_b64_tr_b16 v[78:79], v157 offset:54784
	v_add_f32_e32 v146, v82, v148
	v_add_f32_e32 v146, v83, v146
	v_add_f32_e32 v146, v52, v146
	v_add_f32_e32 v148, v53, v146
	v_cvt_pk_bf16_f32 v146, v80, v81
	v_cvt_pk_bf16_f32 v147, v82, v83
	v_exp_f32_e32 v60, v60
	v_exp_f32_e32 v61, v61
	v_exp_f32_e32 v62, v62
	v_exp_f32_e32 v63, v63
	s_waitcnt lgkmcnt(0)
	v_mfma_f32_32x32x16_bf16 v[100:115], v[202:205], v[128:131], v[100:115]
	ds_read_b128 v[202:205], v156 offset:8192
	ds_read_b64_tr_b16 v[80:81], v157 offset:51200
	ds_read_b64_tr_b16 v[82:83], v157 offset:51712
	v_add_f32_e32 v148, v54, v148
	v_add_f32_e32 v148, v55, v148
	v_add_f32_e32 v148, v56, v148
	v_add_f32_e32 v152, v57, v148
	v_cvt_pk_bf16_f32 v148, v52, v53
	v_cvt_pk_bf16_f32 v149, v54, v55
	v_exp_f32_e32 v64, v64
	v_exp_f32_e32 v65, v65
	v_exp_f32_e32 v66, v66
	v_exp_f32_e32 v67, v67
	v_mfma_f32_32x32x16_bf16 v[84:99], v[190:193], v[128:131], v[84:99]
	ds_read_b128 v[190:193], v156 offset:8704
	ds_read_b64_tr_b16 v[52:53], v157 offset:55296
	ds_read_b64_tr_b16 v[54:55], v157 offset:55808
	v_add_f32_e32 v150, v58, v152
	v_add_f32_e32 v150, v59, v150
	v_add_f32_e32 v150, v60, v150
	v_add_f32_e32 v152, v61, v150
	v_cvt_pk_bf16_f32 v150, v56, v57
	v_cvt_pk_bf16_f32 v151, v58, v59
	v_mfma_f32_32x32x16_bf16 v[100:115], v[194:197], v[124:127], v[100:115]
	ds_read_b128 v[194:197], v156 offset:10240
	ds_read_b64_tr_b16 v[56:57], v157 offset:52224
	ds_read_b64_tr_b16 v[58:59], v157 offset:52736
	v_add_f32_e32 v152, v62, v152
	v_add_f32_e32 v152, v63, v152
	v_add_f32_e32 v152, v64, v152
	v_add_f32_e32 v160, v65, v152
	v_cvt_pk_bf16_f32 v152, v60, v61
	v_cvt_pk_bf16_f32 v153, v62, v63
	v_mfma_f32_32x32x16_bf16 v[84:99], v[198:201], v[124:127], v[84:99]
	ds_read_b128 v[198:201], v156 offset:10752
	ds_read_b64_tr_b16 v[60:61], v157 offset:56320
	ds_read_b64_tr_b16 v[62:63], v157 offset:56832
	v_add_f32_e32 v154, v66, v160
	v_add_f32_e32 v156, v67, v154
	v_cvt_pk_bf16_f32 v154, v64, v65
	v_cvt_pk_bf16_f32 v155, v66, v67
	s_waitcnt lgkmcnt(0)
	v_mfma_f32_32x32x16_bf16 v[100:115], v[202:205], v[120:123], v[100:115]
	v_mfma_f32_32x32x16_bf16 v[84:99], v[190:193], v[120:123], v[84:99]
	v_mfma_f32_32x32x16_bf16 v[100:115], v[194:197], v[116:119], v[100:115]
	v_mfma_f32_32x32x16_bf16 v[84:99], v[198:201], v[116:119], v[84:99]
	s_setprio 0
	s_cmp_lt_i32 s19, s52
	s_cbranch_scc0 .LBB0_1167

.LBB0_1153:
	v_mfma_f32_32x32x16_bf16 v[4:19], v[140:143], v[172:175], v[4:19]
	v_exp_f32_e32 v100, v100
	v_exp_f32_e32 v101, v101
	v_exp_f32_e32 v102, v102
	v_exp_f32_e32 v103, v103
	v_mfma_f32_32x32x16_bf16 v[20:35], v[140:143], v[68:71], v[20:35]
	v_exp_f32_e32 v104, v104
	v_exp_f32_e32 v105, v105
	v_exp_f32_e32 v106, v106
	v_exp_f32_e32 v107, v107
	s_and_b32 s12, s27, 3
	s_mulk_i32 s12, 0x3000
	v_add_u32_e32 v140, s12, v188
	v_lshl_add_u32 v141, s18, 13, v186
	ds_read_b128 v[202:205], v140
	ds_read_b128 v[190:193], v140 offset:512
	ds_read_b128 v[194:197], v140 offset:2048
	ds_read_b128 v[198:201], v140 offset:2560
	v_mfma_f32_32x32x16_bf16 v[4:19], v[144:147], v[72:75], v[4:19]
	v_exp_f32_e32 v108, v108
	v_exp_f32_e32 v109, v109
	v_exp_f32_e32 v110, v110
	v_exp_f32_e32 v111, v111
	v_mfma_f32_32x32x16_bf16 v[20:35], v[144:147], v[76:79], v[20:35]
	v_exp_f32_e32 v112, v112
	v_exp_f32_e32 v113, v113
	v_exp_f32_e32 v114, v114
	v_exp_f32_e32 v115, v115
	v_mfma_f32_32x32x16_bf16 v[4:19], v[148:151], v[80:83], v[4:19]
	v_exp_f32_e32 v84, v84
	v_exp_f32_e32 v85, v85
	v_exp_f32_e32 v86, v86
	v_exp_f32_e32 v87, v87
	v_mfma_f32_32x32x16_bf16 v[20:35], v[148:151], v[52:55], v[20:35]
	v_exp_f32_e32 v88, v88
	v_exp_f32_e32 v89, v89
	v_exp_f32_e32 v90, v90
	v_exp_f32_e32 v91, v91
	v_mfma_f32_32x32x16_bf16 v[4:19], v[152:155], v[56:59], v[4:19]
	v_mfma_f32_32x32x16_bf16 v[20:35], v[152:155], v[60:63], v[20:35]
	s_and_b64 vcc, exec, s[10:11]
	s_cbranch_vccnz .Lmla_resc1
.LBB0_1155:
	s_waitcnt vmcnt(2) lgkmcnt(0)
	s_barrier
.LBB0_1159:
	s_setprio 1
	s_waitcnt lgkmcnt(0)
	v_mfma_f32_32x32x16_bf16 v[68:83], v[202:205], v[136:139], v[36:51]
	s_add_i32 s8, s27, 3
	s_min_i32 s8, s8, s2
	s_lshl_b64 s[10:11], s[8:9], 17
	v_lshl_add_u64 v[170:171], v[176:177], 0, s[10:11]
	s_add_i32 s10, s26, s20
	s_mov_b32 m0, s10
	s_nop 0
	global_load_lds_dwordx4 v[170:171], off
	v_add_f32_e32 v56, v100, v101
	ds_read_b128 v[202:205], v140 offset:4096
	ds_read_b64_tr_b16 v[172:173], v141 offset:49152
	ds_read_b64_tr_b16 v[174:175], v141 offset:49664
	v_add_f32_e32 v52, v102, v56
	v_add_f32_e32 v52, v103, v52
	v_add_f32_e32 v52, v104, v52
	v_add_f32_e32 v144, v105, v52
	v_cvt_pk_bf16_f32 v156, v100, v101
	v_cvt_pk_bf16_f32 v157, v102, v103
	v_mfma_f32_32x32x16_bf16 v[52:67], v[190:193], v[136:139], v[36:51]
	s_and_b64 vcc, exec, s[38:39]
	s_cbranch_vccnz .Lmla_rope2
	s_lshl_b64 s[12:13], s[8:9], 18
	v_lshl_add_u64 v[170:171], v[180:181], 0, s[12:13]
	s_add_i32 m0, s10, 0x2000
	s_nop 0
	global_load_lds_dwordx4 v[170:171], off
.Lmla_rope2:
	ds_read_b128 v[190:193], v140 offset:4608
	ds_read_b64_tr_b16 v[100:101], v141 offset:53248
	ds_read_b64_tr_b16 v[102:103], v141 offset:53760
	v_add_f32_e32 v144, v106, v144
	v_add_f32_e32 v144, v107, v144
	v_add_f32_e32 v144, v108, v144
	v_add_f32_e32 v144, v109, v144
	v_cvt_pk_bf16_f32 v158, v104, v105
	v_cvt_pk_bf16_f32 v159, v106, v107
	v_mfma_f32_32x32x16_bf16 v[68:83], v[194:197], v[132:135], v[68:83]
	s_cmp_lt_u32 s19, s3
	s_cselect_b32 s8, s16, s2
	s_lshl_b64 s[10:11], s[8:9], 17
	v_lshl_add_u64 v[170:171], v[178:179], 0, s[10:11]
	s_add_i32 s8, s26, s17
	v_lshl_add_u64 v[170:171], v[170:171], 0, s[24:25]
	s_add_i32 m0, s8, 0xc000
	s_and_b32 s17, s27, 3
	global_load_lds_dwordx4 v[170:171], off
	s_mulk_i32 s17, 0x3000
	ds_read_b128 v[194:197], v140 offset:6144
	ds_read_b64_tr_b16 v[104:105], v141 offset:50176
	ds_read_b64_tr_b16 v[106:107], v141 offset:50688
	v_add_f32_e32 v144, v110, v144
	v_add_f32_e32 v144, v111, v144
	v_add_f32_e32 v144, v112, v144
	v_add_f32_e32 v144, v113, v144
	v_cvt_pk_bf16_f32 v160, v108, v109
	v_cvt_pk_bf16_f32 v161, v110, v111
	v_mfma_f32_32x32x16_bf16 v[52:67], v[198:201], v[132:135], v[52:67]
	ds_read_b128 v[198:201], v140 offset:6656
	ds_read_b64_tr_b16 v[108:109], v141 offset:54272
	ds_read_b64_tr_b16 v[110:111], v141 offset:54784
	v_add_f32_e32 v144, v114, v144
	v_add_f32_e32 v144, v115, v144
	v_add_f32_e32 v144, v84, v144
	v_add_f32_e32 v144, v85, v144
	v_cvt_pk_bf16_f32 v162, v112, v113
	v_cvt_pk_bf16_f32 v163, v114, v115
	v_exp_f32_e32 v92, v92
	v_exp_f32_e32 v93, v93
	v_exp_f32_e32 v94, v94
	v_exp_f32_e32 v95, v95
	s_waitcnt lgkmcnt(0)
	v_mfma_f32_32x32x16_bf16 v[68:83], v[202:205], v[128:131], v[68:83]
	ds_read_b128 v[202:205], v140 offset:8192
	ds_read_b64_tr_b16 v[112:113], v141 offset:51200
	ds_read_b64_tr_b16 v[114:115], v141 offset:51712
	v_add_f32_e32 v144, v86, v144
	v_add_f32_e32 v144, v87, v144
	v_add_f32_e32 v144, v88, v144
	v_add_f32_e32 v144, v89, v144
	v_cvt_pk_bf16_f32 v164, v84, v85
	v_cvt_pk_bf16_f32 v165, v86, v87
	v_exp_f32_e32 v96, v96
	v_exp_f32_e32 v97, v97
	v_exp_f32_e32 v98, v98
	v_exp_f32_e32 v99, v99
	v_mfma_f32_32x32x16_bf16 v[52:67], v[190:193], v[128:131], v[52:67]
	ds_read_b128 v[190:193], v140 offset:8704
	ds_read_b64_tr_b16 v[84:85], v141 offset:55296
	ds_read_b64_tr_b16 v[86:87], v141 offset:55808
	v_add_f32_e32 v144, v90, v144
	v_add_f32_e32 v144, v91, v144
	v_add_f32_e32 v144, v92, v144
	v_add_f32_e32 v144, v93, v144
	v_cvt_pk_bf16_f32 v166, v88, v89
	v_cvt_pk_bf16_f32 v167, v90, v91
	v_mfma_f32_32x32x16_bf16 v[68:83], v[194:197], v[124:127], v[68:83]
	ds_read_b128 v[194:197], v140 offset:10240
	ds_read_b64_tr_b16 v[88:89], v141 offset:52224
	ds_read_b64_tr_b16 v[90:91], v141 offset:52736
	v_add_f32_e32 v144, v94, v144
	v_add_f32_e32 v144, v95, v144
	v_add_f32_e32 v144, v96, v144
	v_add_f32_e32 v144, v97, v144
	v_cvt_pk_bf16_f32 v168, v92, v93
	v_cvt_pk_bf16_f32 v169, v94, v95
	v_mfma_f32_32x32x16_bf16 v[52:67], v[198:201], v[124:127], v[52:67]
	ds_read_b128 v[198:201], v140 offset:10752
	ds_read_b64_tr_b16 v[92:93], v141 offset:56320
	ds_read_b64_tr_b16 v[94:95], v141 offset:56832
	v_add_f32_e32 v140, v98, v144
	v_add_f32_e32 v140, v99, v140
	v_cvt_pk_bf16_f32 v170, v96, v97
	v_cvt_pk_bf16_f32 v171, v98, v99
	s_waitcnt lgkmcnt(0)
	v_mfma_f32_32x32x16_bf16 v[68:83], v[202:205], v[120:123], v[68:83]
	v_mfma_f32_32x32x16_bf16 v[52:67], v[190:193], v[120:123], v[52:67]
	v_mfma_f32_32x32x16_bf16 v[68:83], v[194:197], v[116:119], v[68:83]
	v_mfma_f32_32x32x16_bf16 v[52:67], v[198:201], v[116:119], v[52:67]
	s_setprio 0
	s_cmp_lt_i32 s27, s52
	s_cbranch_scc0 .LBB0_1171

.LBB0_1163:
	v_mfma_f32_32x32x16_bf16 v[4:19], v[156:159], v[172:175], v[4:19]
	v_exp_f32_e32 v68, v68
	v_exp_f32_e32 v69, v69
	v_exp_f32_e32 v70, v70
	v_exp_f32_e32 v71, v71
	v_mfma_f32_32x32x16_bf16 v[20:35], v[156:159], v[100:103], v[20:35]
	v_exp_f32_e32 v72, v72
	v_exp_f32_e32 v73, v73
	v_exp_f32_e32 v74, v74
	v_exp_f32_e32 v75, v75
	s_add_i32 s12, s16, -1
	s_and_b32 s12, s12, 3
	s_mulk_i32 s12, 0x3000
	v_add_u32_e32 v156, s12, v188
	s_add_i32 s12, s14, 0x4000
	s_and_b32 s12, s12, 0x6000
	v_add_u32_e32 v157, s12, v186
	ds_read_b128 v[202:205], v156
	ds_read_b128 v[190:193], v156 offset:512
	ds_read_b128 v[194:197], v156 offset:2048
	ds_read_b128 v[198:201], v156 offset:2560
	v_mfma_f32_32x32x16_bf16 v[4:19], v[160:163], v[104:107], v[4:19]
	v_exp_f32_e32 v76, v76
	v_exp_f32_e32 v77, v77
	v_exp_f32_e32 v78, v78
	v_exp_f32_e32 v79, v79
	v_mfma_f32_32x32x16_bf16 v[20:35], v[160:163], v[108:111], v[20:35]
	v_exp_f32_e32 v80, v80
	v_exp_f32_e32 v81, v81
	v_exp_f32_e32 v82, v82
	v_exp_f32_e32 v83, v83
	v_mfma_f32_32x32x16_bf16 v[4:19], v[164:167], v[112:115], v[4:19]
	v_exp_f32_e32 v52, v52
	v_exp_f32_e32 v53, v53
	v_exp_f32_e32 v54, v54
	v_exp_f32_e32 v55, v55
	v_mfma_f32_32x32x16_bf16 v[20:35], v[164:167], v[84:87], v[20:35]
	v_exp_f32_e32 v56, v56
	v_exp_f32_e32 v57, v57
	v_exp_f32_e32 v58, v58
	v_exp_f32_e32 v59, v59
	v_mfma_f32_32x32x16_bf16 v[4:19], v[168:171], v[88:91], v[4:19]
	v_mfma_f32_32x32x16_bf16 v[20:35], v[168:171], v[92:95], v[20:35]
	s_and_b64 vcc, exec, s[10:11]
	s_cbranch_vccnz .Lmla_resc2

; __device__ __forceinline__ void mla_unit(int b, int h, int qb, const bf16_t* __restrict__ Q, const bf16_t* __restrict__ KV, const bf16_t* __restrict__ PROJ, bf16_t* OCAT, float* SSQO, ldsp shm) {
;     ...
;     int t = 1;
;     for (; t + 1 < NT; t += 2) { STEP(pB0, pB1, pA0, pA1, t); STEP(pA0, pA1, pB0, pB1, t + 1); }
;     STEP(pB0, pB1, pA0, pA1, t);
.LBB0_1179:
	s_add_i32 s3, s17, 0
	s_lshl_b32 s8, s2, 17
	s_add_i32 s3, s3, s34
	v_lshl_add_u64 v[84:85], v[176:177], 0, s[8:9]
	s_mov_b32 m0, s3
	s_and_b64 vcc, exec, s[38:39]
	global_load_lds_dwordx4 v[84:85], off
	s_cbranch_vccnz .LBB0_1181
	s_lshl_b32 s10, s2, 18
	s_mov_b32 s11, s9
	v_lshl_add_u64 v[84:85], v[180:181], 0, s[10:11]
	s_add_i32 m0, s3, 0x2000
	s_nop 0
	global_load_lds_dwordx4 v[84:85], off
.LBB0_1181:
	s_xor_b32 s2, s15, 0x4000
	s_add_i32 s2, s2, 0
	v_lshl_add_u64 v[84:85], v[178:179], 0, s[8:9]
	s_add_i32 s2, s2, s34
	v_lshl_add_u64 v[84:85], v[84:85], 0, s[24:25]
	s_add_i32 m0, s2, 0xc000
	s_and_b32 s2, s12, 3
	global_load_lds_dwordx4 v[84:85], off
	s_mulk_i32 s2, 0x3000
	s_and_b32 s2, s14, 0x6000
	s_setprio 1
	s_waitcnt lgkmcnt(0)
	v_mfma_f32_32x32x16_bf16 v[84:99], v[202:205], v[136:139], v[36:51]
	v_add_f32_e32 v144, v68, v69
	ds_read_b128 v[140:143], v156 offset:4096
	ds_read_b64_tr_b16 v[100:101], v157 offset:49152
	ds_read_b64_tr_b16 v[102:103], v157 offset:49664
	v_add_f32_e32 v144, v70, v144
	v_add_f32_e32 v144, v71, v144
	v_add_f32_e32 v144, v72, v144
	v_add_f32_e32 v144, v73, v144
	v_cvt_pk_bf16_f32 v68, v68, v69
	v_cvt_pk_bf16_f32 v69, v70, v71
	v_mfma_f32_32x32x16_bf16 v[36:51], v[190:193], v[136:139], v[36:51]
	ds_read_b128 v[136:139], v156 offset:4608
	ds_read_b64_tr_b16 v[104:105], v157 offset:53248
	ds_read_b64_tr_b16 v[106:107], v157 offset:53760
	v_add_f32_e32 v70, v74, v144
	v_add_f32_e32 v70, v75, v70
	v_add_f32_e32 v70, v76, v70
	v_add_f32_e32 v148, v77, v70
	v_cvt_pk_bf16_f32 v70, v72, v73
	v_cvt_pk_bf16_f32 v71, v74, v75
	v_mfma_f32_32x32x16_bf16 v[84:99], v[194:197], v[132:135], v[84:99]
	ds_read_b128 v[144:147], v156 offset:6144
	ds_read_b64_tr_b16 v[108:109], v157 offset:50176
	ds_read_b64_tr_b16 v[110:111], v157 offset:50688
	v_add_f32_e32 v72, v78, v148
	v_add_f32_e32 v72, v79, v72
	v_add_f32_e32 v72, v80, v72
	v_add_f32_e32 v152, v81, v72
	v_cvt_pk_bf16_f32 v72, v76, v77
	v_cvt_pk_bf16_f32 v73, v78, v79
	v_mfma_f32_32x32x16_bf16 v[36:51], v[198:201], v[132:135], v[36:51]
	ds_read_b128 v[148:151], v156 offset:6656
	ds_read_b64_tr_b16 v[76:77], v157 offset:54272
	ds_read_b64_tr_b16 v[78:79], v157 offset:54784
	v_add_f32_e32 v74, v82, v152
	v_add_f32_e32 v74, v83, v74
	v_add_f32_e32 v74, v52, v74
	v_add_f32_e32 v132, v53, v74
	v_cvt_pk_bf16_f32 v74, v80, v81
	v_cvt_pk_bf16_f32 v75, v82, v83
	v_exp_f32_e32 v60, v60
	v_exp_f32_e32 v61, v61
	v_exp_f32_e32 v62, v62
	v_exp_f32_e32 v63, v63
	s_waitcnt lgkmcnt(0)
	v_mfma_f32_32x32x16_bf16 v[84:99], v[140:143], v[128:131], v[84:99]
	ds_read_b128 v[140:143], v156 offset:8192
	ds_read_b64_tr_b16 v[112:113], v157 offset:51200
	ds_read_b64_tr_b16 v[114:115], v157 offset:51712
	v_add_f32_e32 v80, v54, v132
	v_add_f32_e32 v80, v55, v80
	v_add_f32_e32 v80, v56, v80
	v_add_f32_e32 v132, v57, v80
	v_cvt_pk_bf16_f32 v80, v52, v53
	v_cvt_pk_bf16_f32 v81, v54, v55
	v_exp_f32_e32 v64, v64
	v_exp_f32_e32 v65, v65
	v_exp_f32_e32 v66, v66
	v_exp_f32_e32 v67, v67
	v_mfma_f32_32x32x16_bf16 v[36:51], v[136:139], v[128:131], v[36:51]
	ds_read_b128 v[152:155], v156 offset:8704
	ds_read_b64_tr_b16 v[128:129], v157 offset:55296
	ds_read_b64_tr_b16 v[130:131], v157 offset:55808
	v_add_f32_e32 v52, v58, v132
	v_add_f32_e32 v52, v59, v52
	v_add_f32_e32 v52, v60, v52
	v_add_f32_e32 v52, v61, v52
	v_cvt_pk_bf16_f32 v82, v56, v57
	v_cvt_pk_bf16_f32 v83, v58, v59
	v_mfma_f32_32x32x16_bf16 v[84:99], v[144:147], v[124:127], v[84:99]
	ds_read_b128 v[54:57], v156 offset:10240
	ds_read_b64_tr_b16 v[136:137], v157 offset:52224
	ds_read_b64_tr_b16 v[138:139], v157 offset:52736
	v_add_f32_e32 v52, v62, v52
	v_add_f32_e32 v52, v63, v52
	v_add_f32_e32 v52, v64, v52
	v_add_f32_e32 v52, v65, v52
	v_cvt_pk_bf16_f32 v132, v60, v61
	v_cvt_pk_bf16_f32 v133, v62, v63
	v_mfma_f32_32x32x16_bf16 v[36:51], v[148:151], v[124:127], v[36:51]
	ds_read_b128 v[58:61], v156 offset:10752
	ds_read_b64_tr_b16 v[124:125], v157 offset:56320
	ds_read_b64_tr_b16 v[126:127], v157 offset:56832
	v_add_f32_e32 v52, v66, v52
	v_add_f32_e32 v52, v67, v52
	v_cvt_pk_bf16_f32 v134, v64, v65
	v_cvt_pk_bf16_f32 v135, v66, v67
	s_waitcnt lgkmcnt(0)
	v_mfma_f32_32x32x16_bf16 v[84:99], v[140:143], v[120:123], v[84:99]
	v_mfma_f32_32x32x16_bf16 v[36:51], v[152:155], v[120:123], v[36:51]
	v_mfma_f32_32x32x16_bf16 v[84:99], v[54:57], v[116:119], v[84:99]
	v_mfma_f32_32x32x16_bf16 v[36:51], v[58:61], v[116:119], v[36:51]
	s_setprio 0
	s_cmp_lt_i32 s12, s52
	s_cbranch_scc0 .LBB0_1195
